# baseline (speedup 1.0000x reference)
.LBB7_26:
	s_lshl_b32 s34, s70, 8
	s_add_i32 s34, s34, s48
	v_or_b32_e32 v250, s34, v165
	v_ashrrev_i32_e32 v251, 31, v250
	v_lshl_add_u64 v[250:251], v[250:251], 3, s[12:13]
	s_lshl_b32 s35, s67, 8
	s_or_b32 s35, s35, s51
	v_or_b32_e32 v252, s35, v164
	v_ashrrev_i32_e32 v253, 31, v252
	v_lshl_add_u64 v[252:253], v[252:253], 2, s[14:15]
	global_load_dword v226, v[250:251], off offset:4
	global_load_dword v227, v[250:251], off offset:132
	global_load_dword v228, v[250:251], off offset:260
	global_load_dword v229, v[250:251], off offset:388
	global_load_dword v230, v[250:251], off offset:1028
	global_load_dword v231, v[250:251], off offset:1156
	global_load_dword v232, v[250:251], off offset:1284
	global_load_dword v233, v[250:251], off offset:1412
	global_load_dwordx4 v[234:237], v[252:253], off
	global_load_dwordx4 v[238:241], v[252:253], off offset:16
	global_load_dwordx4 v[242:245], v[252:253], off offset:128
	global_load_dwordx4 v[246:249], v[252:253], off offset:144
	s_add_u32 s28, s28, 0x30080
	s_addc_u32 s29, s29, 0
	s_add_u32 s71, s30, 0x100
	v_mov_b32_e32 v0, 0
	s_addc_u32 s72, s31, 0
	s_mov_b32 s73, -2
	v_mov_b32_e32 v1, v0
	v_mov_b32_e32 v2, v0
	v_mov_b32_e32 v3, v0
	v_mov_b32_e32 v4, v0
	v_mov_b32_e32 v5, v0
	v_mov_b32_e32 v6, v0
	v_mov_b32_e32 v7, v0
	v_mov_b32_e32 v12, v0
	v_mov_b32_e32 v13, v0
	v_mov_b32_e32 v14, v0
	v_mov_b32_e32 v15, v0
	v_mov_b32_e32 v20, v0
	v_mov_b32_e32 v21, v0
	v_mov_b32_e32 v22, v0
	v_mov_b32_e32 v23, v0
	v_mov_b32_e32 v28, v0
	v_mov_b32_e32 v29, v0
	v_mov_b32_e32 v30, v0
	v_mov_b32_e32 v31, v0
	v_mov_b32_e32 v36, v0
	v_mov_b32_e32 v37, v0
	v_mov_b32_e32 v38, v0
	v_mov_b32_e32 v39, v0
	v_mov_b32_e32 v44, v0
	v_mov_b32_e32 v45, v0
	v_mov_b32_e32 v46, v0
	v_mov_b32_e32 v47, v0
	v_mov_b32_e32 v52, v0
	v_mov_b32_e32 v53, v0
	v_mov_b32_e32 v54, v0
	v_mov_b32_e32 v55, v0
	v_mov_b32_e32 v8, v0
	v_mov_b32_e32 v9, v0
	v_mov_b32_e32 v10, v0
	v_mov_b32_e32 v11, v0
	v_mov_b32_e32 v16, v0
	v_mov_b32_e32 v17, v0
	v_mov_b32_e32 v18, v0
	v_mov_b32_e32 v19, v0
	v_mov_b32_e32 v24, v0
	v_mov_b32_e32 v25, v0
	v_mov_b32_e32 v26, v0
	v_mov_b32_e32 v27, v0
	v_mov_b32_e32 v32, v0
	v_mov_b32_e32 v33, v0
	v_mov_b32_e32 v34, v0
	v_mov_b32_e32 v35, v0
	v_mov_b32_e32 v40, v0
	v_mov_b32_e32 v41, v0
	v_mov_b32_e32 v42, v0
	v_mov_b32_e32 v43, v0
	v_mov_b32_e32 v48, v0
	v_mov_b32_e32 v49, v0
	v_mov_b32_e32 v50, v0
	v_mov_b32_e32 v51, v0
	v_mov_b32_e32 v56, v0
	v_mov_b32_e32 v57, v0
	v_mov_b32_e32 v58, v0
	v_mov_b32_e32 v59, v0
	v_mov_b32_e32 v60, v0
	v_mov_b32_e32 v61, v0
	v_mov_b32_e32 v62, v0
	v_mov_b32_e32 v63, v0
	v_mov_b32_e32 v64, v0
	v_mov_b32_e32 v65, v0
	v_mov_b32_e32 v66, v0
	v_mov_b32_e32 v67, v0
	v_mov_b32_e32 v68, v0
	v_mov_b32_e32 v69, v0
	v_mov_b32_e32 v70, v0
	v_mov_b32_e32 v71, v0
	v_mov_b32_e32 v76, v0
	v_mov_b32_e32 v77, v0
	v_mov_b32_e32 v78, v0
	v_mov_b32_e32 v79, v0
	v_mov_b32_e32 v84, v0
	v_mov_b32_e32 v85, v0
	v_mov_b32_e32 v86, v0
	v_mov_b32_e32 v87, v0
	v_mov_b32_e32 v92, v0
	v_mov_b32_e32 v93, v0
	v_mov_b32_e32 v94, v0
	v_mov_b32_e32 v95, v0
	v_mov_b32_e32 v100, v0
	v_mov_b32_e32 v101, v0
	v_mov_b32_e32 v102, v0
	v_mov_b32_e32 v103, v0
	v_mov_b32_e32 v112, v0
	v_mov_b32_e32 v113, v0
	v_mov_b32_e32 v114, v0
	v_mov_b32_e32 v115, v0
	v_mov_b32_e32 v116, v0
	v_mov_b32_e32 v117, v0
	v_mov_b32_e32 v118, v0
	v_mov_b32_e32 v119, v0
	v_mov_b32_e32 v72, v0
	v_mov_b32_e32 v73, v0
	v_mov_b32_e32 v74, v0
	v_mov_b32_e32 v75, v0
	v_mov_b32_e32 v80, v0
	v_mov_b32_e32 v81, v0
	v_mov_b32_e32 v82, v0
	v_mov_b32_e32 v83, v0
	v_mov_b32_e32 v88, v0
	v_mov_b32_e32 v89, v0
	v_mov_b32_e32 v90, v0
	v_mov_b32_e32 v91, v0
	v_mov_b32_e32 v96, v0
	v_mov_b32_e32 v97, v0
	v_mov_b32_e32 v98, v0
	v_mov_b32_e32 v99, v0
	v_mov_b32_e32 v104, v0
	v_mov_b32_e32 v105, v0
	v_mov_b32_e32 v106, v0
	v_mov_b32_e32 v107, v0
	v_mov_b32_e32 v108, v0
	v_mov_b32_e32 v109, v0
	v_mov_b32_e32 v110, v0
	v_mov_b32_e32 v111, v0
	v_mov_b32_e32 v120, v0
	v_mov_b32_e32 v121, v0
	v_mov_b32_e32 v122, v0
	v_mov_b32_e32 v123, v0
	v_mov_b32_e32 v124, v0
	v_mov_b32_e32 v125, v0
	v_mov_b32_e32 v126, v0
	v_mov_b32_e32 v127, v0
	.p2alignl 6, 3212836864

.LBB7_32:
	s_endpgm
	s_endpgm
	s_endpgm
	s_endpgm
	s_endpgm
	s_endpgm
	s_endpgm
	s_endpgm
	s_endpgm
	s_endpgm
	s_endpgm
	s_endpgm
	s_endpgm
	s_endpgm
	s_endpgm
	s_endpgm
	s_endpgm
	s_endpgm
	s_endpgm
	s_endpgm
	s_endpgm
	s_endpgm
	s_endpgm
	s_endpgm
	s_endpgm
	s_endpgm
	s_endpgm
	s_endpgm
	s_endpgm
	s_endpgm
	s_endpgm
	s_endpgm
	s_endpgm
	s_endpgm
	s_endpgm
	s_endpgm
	s_endpgm
	s_endpgm
	s_endpgm
	s_endpgm
	s_endpgm
	s_endpgm
	s_endpgm
	s_endpgm
	s_endpgm
	.section	.rodata,"a",@progbits
	.p2align	6, 0x0

.LBB8_26:
	s_add_u32 s38, s38, 0x30080
	s_addc_u32 s39, s39, 0
	s_add_u32 s85, s40, 0x100
	v_mov_b32_e32 v0, 0
	s_addc_u32 s86, s41, 0
	s_mov_b32 s87, -2
	v_mov_b32_e32 v1, v0
	v_mov_b32_e32 v2, v0
	v_mov_b32_e32 v3, v0
	v_mov_b32_e32 v4, v0
	v_mov_b32_e32 v5, v0
	v_mov_b32_e32 v6, v0
	v_mov_b32_e32 v7, v0
	v_mov_b32_e32 v16, v0
	v_mov_b32_e32 v17, v0
	v_mov_b32_e32 v18, v0
	v_mov_b32_e32 v19, v0
	v_mov_b32_e32 v20, v0
	v_mov_b32_e32 v21, v0
	v_mov_b32_e32 v22, v0
	v_mov_b32_e32 v23, v0
	v_mov_b32_e32 v32, v0
	v_mov_b32_e32 v33, v0
	v_mov_b32_e32 v34, v0
	v_mov_b32_e32 v35, v0
	v_mov_b32_e32 v36, v0
	v_mov_b32_e32 v37, v0
	v_mov_b32_e32 v38, v0
	v_mov_b32_e32 v39, v0
	v_mov_b32_e32 v48, v0
	v_mov_b32_e32 v49, v0
	v_mov_b32_e32 v50, v0
	v_mov_b32_e32 v51, v0
	v_mov_b32_e32 v52, v0
	v_mov_b32_e32 v53, v0
	v_mov_b32_e32 v54, v0
	v_mov_b32_e32 v55, v0
	v_mov_b32_e32 v8, v0
	v_mov_b32_e32 v9, v0
	v_mov_b32_e32 v10, v0
	v_mov_b32_e32 v11, v0
	v_mov_b32_e32 v12, v0
	v_mov_b32_e32 v13, v0
	v_mov_b32_e32 v14, v0
	v_mov_b32_e32 v15, v0
	v_mov_b32_e32 v24, v0
	v_mov_b32_e32 v25, v0
	v_mov_b32_e32 v26, v0
	v_mov_b32_e32 v27, v0
	v_mov_b32_e32 v28, v0
	v_mov_b32_e32 v29, v0
	v_mov_b32_e32 v30, v0
	v_mov_b32_e32 v31, v0
	v_mov_b32_e32 v40, v0
	v_mov_b32_e32 v41, v0
	v_mov_b32_e32 v42, v0
	v_mov_b32_e32 v43, v0
	v_mov_b32_e32 v44, v0
	v_mov_b32_e32 v45, v0
	v_mov_b32_e32 v46, v0
	v_mov_b32_e32 v47, v0
	v_mov_b32_e32 v56, v0
	v_mov_b32_e32 v57, v0
	v_mov_b32_e32 v58, v0
	v_mov_b32_e32 v59, v0
	v_mov_b32_e32 v60, v0
	v_mov_b32_e32 v61, v0
	v_mov_b32_e32 v62, v0
	v_mov_b32_e32 v63, v0
	v_mov_b32_e32 v64, v0
	v_mov_b32_e32 v65, v0
	v_mov_b32_e32 v66, v0
	v_mov_b32_e32 v67, v0
	v_mov_b32_e32 v68, v0
	v_mov_b32_e32 v69, v0
	v_mov_b32_e32 v70, v0
	v_mov_b32_e32 v71, v0
	v_mov_b32_e32 v96, v0
	v_mov_b32_e32 v97, v0
	v_mov_b32_e32 v98, v0
	v_mov_b32_e32 v99, v0
	v_mov_b32_e32 v100, v0
	v_mov_b32_e32 v101, v0
	v_mov_b32_e32 v102, v0
	v_mov_b32_e32 v103, v0
	v_mov_b32_e32 v112, v0
	v_mov_b32_e32 v113, v0
	v_mov_b32_e32 v114, v0
	v_mov_b32_e32 v115, v0
	v_mov_b32_e32 v116, v0
	v_mov_b32_e32 v117, v0
	v_mov_b32_e32 v118, v0
	v_mov_b32_e32 v119, v0
	v_mov_b32_e32 v128, v0
	v_mov_b32_e32 v129, v0
	v_mov_b32_e32 v130, v0
	v_mov_b32_e32 v131, v0
	v_mov_b32_e32 v132, v0
	v_mov_b32_e32 v133, v0
	v_mov_b32_e32 v134, v0
	v_mov_b32_e32 v135, v0
	v_mov_b32_e32 v76, v0
	v_mov_b32_e32 v77, v0
	v_mov_b32_e32 v78, v0
	v_mov_b32_e32 v79, v0
	v_mov_b32_e32 v84, v0
	v_mov_b32_e32 v85, v0
	v_mov_b32_e32 v86, v0
	v_mov_b32_e32 v87, v0
	v_mov_b32_e32 v104, v0
	v_mov_b32_e32 v105, v0
	v_mov_b32_e32 v106, v0
	v_mov_b32_e32 v107, v0
	v_mov_b32_e32 v108, v0
	v_mov_b32_e32 v109, v0
	v_mov_b32_e32 v110, v0
	v_mov_b32_e32 v111, v0
	v_mov_b32_e32 v120, v0
	v_mov_b32_e32 v121, v0
	v_mov_b32_e32 v122, v0
	v_mov_b32_e32 v123, v0
	v_mov_b32_e32 v124, v0
	v_mov_b32_e32 v125, v0
	v_mov_b32_e32 v126, v0
	v_mov_b32_e32 v127, v0
	v_mov_b32_e32 v140, v0
	v_mov_b32_e32 v141, v0
	v_mov_b32_e32 v142, v0
	v_mov_b32_e32 v143, v0
	v_mov_b32_e32 v144, v0
	v_mov_b32_e32 v145, v0
	v_mov_b32_e32 v146, v0
	v_mov_b32_e32 v147, v0
	.p2alignl 6, 3212836864

.LBB8_32:
	s_endpgm
	s_endpgm
	s_endpgm
	s_endpgm
	s_endpgm
	s_endpgm
	s_endpgm
	s_endpgm
	s_endpgm
	s_endpgm
	s_endpgm
	s_endpgm
	s_endpgm
	s_endpgm
	s_endpgm
	s_endpgm
	s_endpgm
	s_endpgm
	s_endpgm
	s_endpgm
	s_endpgm
	s_endpgm
	s_endpgm
	s_endpgm
	s_endpgm
	s_endpgm
	s_endpgm
	s_endpgm
	s_endpgm
	s_endpgm
	s_endpgm
	s_endpgm
	.section	.rodata,"a",@progbits
	.p2align	6, 0x0

.LBB9_26:
	s_lshl_b32 s34, s70, 8
	s_add_i32 s34, s34, s48
	v_or_b32_e32 v250, s34, v167
	v_ashrrev_i32_e32 v251, 31, v250
	v_lshl_add_u64 v[250:251], v[250:251], 3, s[12:13]
	s_lshl_b32 s35, s68, 8
	s_or_b32 s35, s35, s51
	v_or_b32_e32 v252, s35, v166
	v_ashrrev_i32_e32 v253, 31, v252
	v_lshl_add_u64 v[252:253], v[252:253], 2, s[14:15]
	global_load_dword v226, v[250:251], off offset:4
	global_load_dword v227, v[250:251], off offset:132
	global_load_dword v228, v[250:251], off offset:260
	global_load_dword v229, v[250:251], off offset:388
	global_load_dword v230, v[250:251], off offset:1028
	global_load_dword v231, v[250:251], off offset:1156
	global_load_dword v232, v[250:251], off offset:1284
	global_load_dword v233, v[250:251], off offset:1412
	global_load_dwordx4 v[234:237], v[252:253], off
	global_load_dwordx4 v[238:241], v[252:253], off offset:16
	global_load_dwordx4 v[242:245], v[252:253], off offset:128
	global_load_dwordx4 v[246:249], v[252:253], off offset:144
	s_add_u32 s28, s28, 0x30080
	s_addc_u32 s29, s29, 0
	s_add_u32 s71, s30, 0x100
	v_mov_b32_e32 v0, 0
	s_addc_u32 s72, s31, 0
	s_mov_b32 s73, -2
	v_mov_b32_e32 v1, v0
	v_mov_b32_e32 v2, v0
	v_mov_b32_e32 v3, v0
	v_mov_b32_e32 v4, v0
	v_mov_b32_e32 v5, v0
	v_mov_b32_e32 v6, v0
	v_mov_b32_e32 v7, v0
	v_mov_b32_e32 v12, v0
	v_mov_b32_e32 v13, v0
	v_mov_b32_e32 v14, v0
	v_mov_b32_e32 v15, v0
	v_mov_b32_e32 v20, v0
	v_mov_b32_e32 v21, v0
	v_mov_b32_e32 v22, v0
	v_mov_b32_e32 v23, v0
	v_mov_b32_e32 v28, v0
	v_mov_b32_e32 v29, v0
	v_mov_b32_e32 v30, v0
	v_mov_b32_e32 v31, v0
	v_mov_b32_e32 v36, v0
	v_mov_b32_e32 v37, v0
	v_mov_b32_e32 v38, v0
	v_mov_b32_e32 v39, v0
	v_mov_b32_e32 v44, v0
	v_mov_b32_e32 v45, v0
	v_mov_b32_e32 v46, v0
	v_mov_b32_e32 v47, v0
	v_mov_b32_e32 v52, v0
	v_mov_b32_e32 v53, v0
	v_mov_b32_e32 v54, v0
	v_mov_b32_e32 v55, v0
	v_mov_b32_e32 v8, v0
	v_mov_b32_e32 v9, v0
	v_mov_b32_e32 v10, v0
	v_mov_b32_e32 v11, v0
	v_mov_b32_e32 v16, v0
	v_mov_b32_e32 v17, v0
	v_mov_b32_e32 v18, v0
	v_mov_b32_e32 v19, v0
	v_mov_b32_e32 v24, v0
	v_mov_b32_e32 v25, v0
	v_mov_b32_e32 v26, v0
	v_mov_b32_e32 v27, v0
	v_mov_b32_e32 v32, v0
	v_mov_b32_e32 v33, v0
	v_mov_b32_e32 v34, v0
	v_mov_b32_e32 v35, v0
	v_mov_b32_e32 v40, v0
	v_mov_b32_e32 v41, v0
	v_mov_b32_e32 v42, v0
	v_mov_b32_e32 v43, v0
	v_mov_b32_e32 v48, v0
	v_mov_b32_e32 v49, v0
	v_mov_b32_e32 v50, v0
	v_mov_b32_e32 v51, v0
	v_mov_b32_e32 v56, v0
	v_mov_b32_e32 v57, v0
	v_mov_b32_e32 v58, v0
	v_mov_b32_e32 v59, v0
	v_mov_b32_e32 v60, v0
	v_mov_b32_e32 v61, v0
	v_mov_b32_e32 v62, v0
	v_mov_b32_e32 v63, v0
	v_mov_b32_e32 v64, v0
	v_mov_b32_e32 v65, v0
	v_mov_b32_e32 v66, v0
	v_mov_b32_e32 v67, v0
	v_mov_b32_e32 v68, v0
	v_mov_b32_e32 v69, v0
	v_mov_b32_e32 v70, v0
	v_mov_b32_e32 v71, v0
	v_mov_b32_e32 v76, v0
	v_mov_b32_e32 v77, v0
	v_mov_b32_e32 v78, v0
	v_mov_b32_e32 v79, v0
	v_mov_b32_e32 v84, v0
	v_mov_b32_e32 v85, v0
	v_mov_b32_e32 v86, v0
	v_mov_b32_e32 v87, v0
	v_mov_b32_e32 v92, v0
	v_mov_b32_e32 v93, v0
	v_mov_b32_e32 v94, v0
	v_mov_b32_e32 v95, v0
	v_mov_b32_e32 v100, v0
	v_mov_b32_e32 v101, v0
	v_mov_b32_e32 v102, v0
	v_mov_b32_e32 v103, v0
	v_mov_b32_e32 v112, v0
	v_mov_b32_e32 v113, v0
	v_mov_b32_e32 v114, v0
	v_mov_b32_e32 v115, v0
	v_mov_b32_e32 v116, v0
	v_mov_b32_e32 v117, v0
	v_mov_b32_e32 v118, v0
	v_mov_b32_e32 v119, v0
	v_mov_b32_e32 v72, v0
	v_mov_b32_e32 v73, v0
	v_mov_b32_e32 v74, v0
	v_mov_b32_e32 v75, v0
	v_mov_b32_e32 v80, v0
	v_mov_b32_e32 v81, v0
	v_mov_b32_e32 v82, v0
	v_mov_b32_e32 v83, v0
	v_mov_b32_e32 v88, v0
	v_mov_b32_e32 v89, v0
	v_mov_b32_e32 v90, v0
	v_mov_b32_e32 v91, v0
	v_mov_b32_e32 v96, v0
	v_mov_b32_e32 v97, v0
	v_mov_b32_e32 v98, v0
	v_mov_b32_e32 v99, v0
	v_mov_b32_e32 v104, v0
	v_mov_b32_e32 v105, v0
	v_mov_b32_e32 v106, v0
	v_mov_b32_e32 v107, v0
	v_mov_b32_e32 v108, v0
	v_mov_b32_e32 v109, v0
	v_mov_b32_e32 v110, v0
	v_mov_b32_e32 v111, v0
	v_mov_b32_e32 v120, v0
	v_mov_b32_e32 v121, v0
	v_mov_b32_e32 v122, v0
	v_mov_b32_e32 v123, v0
	v_mov_b32_e32 v124, v0
	v_mov_b32_e32 v125, v0
	v_mov_b32_e32 v126, v0
	v_mov_b32_e32 v127, v0
	.p2alignl 6, 3212836864

.LBB9_32:
	s_endpgm
	s_endpgm
	s_endpgm
	s_endpgm
	s_endpgm
	s_endpgm
	s_endpgm
	s_endpgm
	s_endpgm
	s_endpgm
	s_endpgm
	s_endpgm
	s_endpgm
	s_endpgm
	s_endpgm
	s_endpgm
	s_endpgm
	s_endpgm
	s_endpgm
	s_endpgm
	s_endpgm
	s_endpgm
	s_endpgm
	s_endpgm
	s_endpgm
	s_endpgm
	s_endpgm
	s_endpgm
	s_endpgm
	s_endpgm
	s_endpgm
	s_endpgm
	s_endpgm
	s_endpgm
	s_endpgm
	s_endpgm
	s_endpgm
	s_endpgm
	s_endpgm
	s_endpgm
	s_endpgm
	s_endpgm
	s_endpgm
	s_endpgm
	s_endpgm
	s_endpgm
	s_endpgm
	.section	.rodata,"a",@progbits
	.p2align	6, 0x0

.LBB10_26:
	s_add_u32 s38, s38, 0xc0080
	s_addc_u32 s39, s39, 0
	s_add_u32 s85, s40, 0x100
	v_mov_b32_e32 v0, 0
	s_addc_u32 s86, s41, 0
	s_mov_b32 s87, -2
	v_mov_b32_e32 v1, v0
	v_mov_b32_e32 v2, v0
	v_mov_b32_e32 v3, v0
	v_mov_b32_e32 v4, v0
	v_mov_b32_e32 v5, v0
	v_mov_b32_e32 v6, v0
	v_mov_b32_e32 v7, v0
	v_mov_b32_e32 v16, v0
	v_mov_b32_e32 v17, v0
	v_mov_b32_e32 v18, v0
	v_mov_b32_e32 v19, v0
	v_mov_b32_e32 v20, v0
	v_mov_b32_e32 v21, v0
	v_mov_b32_e32 v22, v0
	v_mov_b32_e32 v23, v0
	v_mov_b32_e32 v32, v0
	v_mov_b32_e32 v33, v0
	v_mov_b32_e32 v34, v0
	v_mov_b32_e32 v35, v0
	v_mov_b32_e32 v36, v0
	v_mov_b32_e32 v37, v0
	v_mov_b32_e32 v38, v0
	v_mov_b32_e32 v39, v0
	v_mov_b32_e32 v48, v0
	v_mov_b32_e32 v49, v0
	v_mov_b32_e32 v50, v0
	v_mov_b32_e32 v51, v0
	v_mov_b32_e32 v52, v0
	v_mov_b32_e32 v53, v0
	v_mov_b32_e32 v54, v0
	v_mov_b32_e32 v55, v0
	v_mov_b32_e32 v8, v0
	v_mov_b32_e32 v9, v0
	v_mov_b32_e32 v10, v0
	v_mov_b32_e32 v11, v0
	v_mov_b32_e32 v12, v0
	v_mov_b32_e32 v13, v0
	v_mov_b32_e32 v14, v0
	v_mov_b32_e32 v15, v0
	v_mov_b32_e32 v24, v0
	v_mov_b32_e32 v25, v0
	v_mov_b32_e32 v26, v0
	v_mov_b32_e32 v27, v0
	v_mov_b32_e32 v28, v0
	v_mov_b32_e32 v29, v0
	v_mov_b32_e32 v30, v0
	v_mov_b32_e32 v31, v0
	v_mov_b32_e32 v40, v0
	v_mov_b32_e32 v41, v0
	v_mov_b32_e32 v42, v0
	v_mov_b32_e32 v43, v0
	v_mov_b32_e32 v44, v0
	v_mov_b32_e32 v45, v0
	v_mov_b32_e32 v46, v0
	v_mov_b32_e32 v47, v0
	v_mov_b32_e32 v56, v0
	v_mov_b32_e32 v57, v0
	v_mov_b32_e32 v58, v0
	v_mov_b32_e32 v59, v0
	v_mov_b32_e32 v60, v0
	v_mov_b32_e32 v61, v0
	v_mov_b32_e32 v62, v0
	v_mov_b32_e32 v63, v0
	v_mov_b32_e32 v64, v0
	v_mov_b32_e32 v65, v0
	v_mov_b32_e32 v66, v0
	v_mov_b32_e32 v67, v0
	v_mov_b32_e32 v68, v0
	v_mov_b32_e32 v69, v0
	v_mov_b32_e32 v70, v0
	v_mov_b32_e32 v71, v0
	v_mov_b32_e32 v96, v0
	v_mov_b32_e32 v97, v0
	v_mov_b32_e32 v98, v0
	v_mov_b32_e32 v99, v0
	v_mov_b32_e32 v100, v0
	v_mov_b32_e32 v101, v0
	v_mov_b32_e32 v102, v0
	v_mov_b32_e32 v103, v0
	v_mov_b32_e32 v112, v0
	v_mov_b32_e32 v113, v0
	v_mov_b32_e32 v114, v0
	v_mov_b32_e32 v115, v0
	v_mov_b32_e32 v116, v0
	v_mov_b32_e32 v117, v0
	v_mov_b32_e32 v118, v0
	v_mov_b32_e32 v119, v0
	v_mov_b32_e32 v128, v0
	v_mov_b32_e32 v129, v0
	v_mov_b32_e32 v130, v0
	v_mov_b32_e32 v131, v0
	v_mov_b32_e32 v132, v0
	v_mov_b32_e32 v133, v0
	v_mov_b32_e32 v134, v0
	v_mov_b32_e32 v135, v0
	v_mov_b32_e32 v76, v0
	v_mov_b32_e32 v77, v0
	v_mov_b32_e32 v78, v0
	v_mov_b32_e32 v79, v0
	v_mov_b32_e32 v84, v0
	v_mov_b32_e32 v85, v0
	v_mov_b32_e32 v86, v0
	v_mov_b32_e32 v87, v0
	v_mov_b32_e32 v104, v0
	v_mov_b32_e32 v105, v0
	v_mov_b32_e32 v106, v0
	v_mov_b32_e32 v107, v0
	v_mov_b32_e32 v108, v0
	v_mov_b32_e32 v109, v0
	v_mov_b32_e32 v110, v0
	v_mov_b32_e32 v111, v0
	v_mov_b32_e32 v120, v0
	v_mov_b32_e32 v121, v0
	v_mov_b32_e32 v122, v0
	v_mov_b32_e32 v123, v0
	v_mov_b32_e32 v124, v0
	v_mov_b32_e32 v125, v0
	v_mov_b32_e32 v126, v0
	v_mov_b32_e32 v127, v0
	v_mov_b32_e32 v140, v0
	v_mov_b32_e32 v141, v0
	v_mov_b32_e32 v142, v0
	v_mov_b32_e32 v143, v0
	v_mov_b32_e32 v144, v0
	v_mov_b32_e32 v145, v0
	v_mov_b32_e32 v146, v0
	v_mov_b32_e32 v147, v0
	.p2alignl 6, 3212836864

.LBB10_32:
	s_endpgm
	s_endpgm
	s_endpgm
	s_endpgm
	s_endpgm
	s_endpgm
	s_endpgm
	s_endpgm
	s_endpgm
	s_endpgm
	s_endpgm
	s_endpgm
	s_endpgm
	s_endpgm
	s_endpgm
	s_endpgm
	s_endpgm
	s_endpgm
	s_endpgm
	s_endpgm
	s_endpgm
	s_endpgm
	s_endpgm
	s_endpgm
	s_endpgm
	s_endpgm
	s_endpgm
	s_endpgm
	s_endpgm
	s_endpgm
	s_endpgm
	s_endpgm
	.section	.rodata,"a",@progbits
	.p2align	6, 0x0
